# scan compute waves: LDS waits relaxed to what each consumer needs (QC, S loop), store-draining vmcnt(1) moved out of the chunk loop
# speedup vs baseline: 1.0064x; 1.0064x over previous
; __device__ __forceinline__ void p4_scan(const Args& a, const Frame& F) {
;     ...
;             int c = lane & 15, q = lane >> 4; asm volatile("" : "+v"(c), "+v"(q));
;             const int ta = w, tb = 7 - w, trA = 16 * ta + c, trB = 16 * tb + c;
;             unsigned kadA[8];
; #pragma unroll
;             for (int ks = 0; ks < 4; ++ks)
; #pragma unroll
;                 for (int t = 0; t < 2; ++t) kadA[ks * 2 + t] = (unsigned)((32 * ks + 8 * q + 4 * t + (c >> 2)) * SP + (4 * w + ((c & 3) >> 1)) * 16 + 8 * (c & 1));
;             f32x4 accC[2][3];
; #pragma unroll
;             for (int d2 = 0; d2 < 2; ++d2)
; #pragma unroll
;                 for (int i = 0; i < 3; ++i) accC[d2][i] = (f32x4){0.f, 0.f, 0.f, 0.f};
;             float mcar = 0.f, pbt, ppx;
;             { const int base0 = chunk_base(0); pbt = CH[(hd * 528 + (base0 >> 7)) * 2]; ppx = CH[(hd * 528 + (base0 >> 7)) * 2 + 1]; }
;             LDS_BARRIER();
;             float btot = pbt, pmx = ppx;
;             LDS_BARRIER();
;             const int npA = (ta + 2) >> 1, npB = (tb + 2) >> 1;
;     ...
;                     const float denA = __shfl(acc2A[2][0] + decA * acc3A[2][0], c), denB = __shfl(acc2B[2][0] + decB * acc3B[2][0], c);
;                     const float invA = frcp_(fmaxf(fabsf(denA), emtA)), invB = frcp_(fmaxf(fabsf(denB), emtB));
;                     { bf16* HXs = store ? HX : (bf16*)(a.ws + WS_H2) - (size_t)T * 512;
;                         const int lnh = c + 16 * q, pfh = (lnh >> 2) & 15, pqh = lnh & 3, bah = 4 * (pfh + 16 * pqh);
;                         const int tokA = base + (dir ? 127 - (16 * ta + pfh) : (16 * ta + pfh)), tokB = base + (dir ? 127 - (16 * tb + pfh) : (16 * tb + pfh));
; #pragma unroll
;                         for (int mt = 0; mt < 2; ++mt) { const f32x4 vA = (acc2A[mt] + acc3A[mt] * decA) * invA, vB = (acc2B[mt] + acc3B[mt] * decB) * invB;
;                             u32x2 o; o.x = pg8::cvt_pk_bf16(vA[0], vA[1]); o.y = pg8::cvt_pk_bf16(vA[2], vA[3]);
;                             o.x = (unsigned)__builtin_amdgcn_ds_bpermute(bah, (int)o.x); o.y = (unsigned)__builtin_amdgcn_ds_bpermute(bah, (int)o.y);
;                             *(u32x2*)(HXs + (size_t)tokA * 512 + h * 128 + vs * 32 + 16 * mt + 4 * pqh) = o;
;                             o.x = pg8::cvt_pk_bf16(vB[0], vB[1]); o.y = pg8::cvt_pk_bf16(vB[2], vB[3]);
.LBB0_447:
	s_or_b64 exec, exec, s[10:11]
	s_lshl_b32 s56, s97, 2
	s_and_b32 s4, s56, 28
	s_ashr_i32 s5, s97, 6
	s_add_i32 s4, s4, s5
	s_bfe_u32 s59, s97, 0x10005
	s_and_b32 s55, s5, 3
	s_ashr_i32 s58, s4, 2
	s_lshl_b32 s4, s59, 2
	s_bfe_u32 s54, s97, 0x20003
	s_or_b32 s57, s4, s55
	s_cmp_eq_u32 s59, 0
	s_mov_b64 s[6:7], -1
	s_cselect_b64 s[4:5], -1, 0
	s_and_b64 vcc, exec, s[40:41]
	s_mul_i32 s76, s57, 0x210
	s_cbranch_vccz .LBB0_473
	v_mov_b32_e32 v9, v154
	v_mov_b32_e32 v10, v155
	s_and_b64 s[6:7], s[4:5], exec
	v_lshlrev_b32_e32 v11, 3, v10
	v_lshrrev_b32_e32 v8, 2, v9
	v_add_u32_e32 v12, v8, v11
	v_lshlrev_b32_e32 v8, 3, v9
	s_mov_b32 s6, 0xac00000
	v_and_or_b32 v8, v8, 24, s67
	s_cselect_b32 s77, s6, 0xec00000
	v_mad_u64_u32 v[148:149], s[6:7], v12, s84, v[8:9]
	s_lshl_b32 s87, s58, 8
	s_add_i32 s87, s87, 0x10000
	s_lshl_b32 s6, s59, 7
	s_or_b32 s8, s87, s6
	s_ashr_i32 s6, s8, 7
	s_add_i32 s6, s6, s76
	s_lshl_b32 s6, s6, 1
	s_ashr_i32 s7, s6, 31
	s_lshl_b64 s[6:7], s[6:7], 2
	s_add_u32 s6, s60, s6
	s_addc_u32 s7, s61, s7
	global_load_dwordx2 v[152:153], v145, s[6:7]
	v_add_u32_e32 v147, s65, v9
	v_add_u32_e32 v177, s66, v9
	v_mul_lo_u32 v8, v147, s84
	v_add_u32_e32 v33, 0, v8
	v_mul_lo_u32 v8, v177, s84
	v_lshlrev_b32_e32 v178, 4, v10
	v_add_u32_e32 v34, 0, v8
	v_lshlrev_b32_e32 v8, 2, v147
	v_add_u32_e32 v179, s85, v8
	v_lshlrev_b32_e32 v12, 2, v177
	v_add_u32_e32 v181, s89, v8
	v_lshlrev_b32_e32 v184, 2, v10
	v_add_u32_e32 v8, v178, v9
	v_and_b32_e32 v10, 3, v9
	v_add_u32_e32 v180, s85, v12
	v_add_u32_e32 v182, s89, v12
	v_bfe_u32 v8, v8, 2, 4
	v_lshlrev_b32_e32 v12, 6, v10
	v_lshl_or_b32 v185, v8, 2, v12
	v_or_b32_e32 v12, s65, v8
	s_waitcnt lgkmcnt(0)
	s_barrier
	v_sub_u32_e32 v13, 0x7f, v12
	v_or_b32_e32 v8, s66, v8
	s_waitcnt lgkmcnt(0)
	s_barrier
	s_add_i32 s6, 0, 0x20130
	v_and_b32_e32 v36, 63, v9
	v_cndmask_b32_e64 v186, v13, v12, s[4:5]
	v_sub_u32_e32 v12, 0x7f, v8
	v_lshlrev_b32_e32 v32, 2, v10
	v_mul_lo_u32 v188, v9, s84
	v_add_u32_e32 v35, s6, v178
	v_add_u32_e32 v183, 0, v178
	v_cndmask_b32_e64 v187, v12, v8, s[4:5]
	s_lshl_b32 s6, s55, 7
	s_lshl_b32 s7, s54, 5
	v_add_u32_e32 v37, s80, v11
	v_add_u32_e32 v8, v188, v178
	v_lshlrev_b32_e32 v144, 1, v32
	v_and_or_b32 v32, v162, 64, v36
	s_mov_b32 s11, 0
	v_add_u32_e32 v149, 0x440, v148
	v_add_u32_e32 v171, 0x2200, v148
	v_add_u32_e32 v172, 0x2640, v148
	v_add_u32_e32 v173, 0x4400, v148
	v_add_u32_e32 v174, 0x4840, v148
	v_add_u32_e32 v175, 0x6600, v148
	v_add_u32_e32 v176, 0x6a40, v148
	s_lshl_b32 s33, s58, 13
	s_xor_b32 s88, s8, 0x80
	v_add_u32_e32 v189, v183, v188
	v_add3_u32 v190, s82, v188, v11
	v_add3_u32 v191, s83, v188, v11
	v_add_u32_e32 v192, 0x2200, v8
	v_add_u32_e32 v193, s90, v8
	v_mov_b32_e32 v201, 0
	v_mov_b32_e32 v8, 0
	v_mov_b32_e32 v9, 0
	v_mov_b32_e32 v10, 0
	v_mov_b32_e32 v11, 0
	v_mov_b32_e32 v12, 0
	v_mov_b32_e32 v13, 0
	v_mov_b32_e32 v14, 0
	v_mov_b32_e32 v15, 0
	v_mov_b32_e32 v16, 0
	v_mov_b32_e32 v17, 0
	v_mov_b32_e32 v18, 0
	v_mov_b32_e32 v19, 0
	v_mov_b32_e32 v20, 0
	v_mov_b32_e32 v21, 0
	v_mov_b32_e32 v22, 0
	v_mov_b32_e32 v23, 0
	v_mov_b32_e32 v24, 0
	v_mov_b32_e32 v25, 0
	v_mov_b32_e32 v26, 0
	v_mov_b32_e32 v27, 0
	v_mov_b32_e32 v28, 0
	v_mov_b32_e32 v29, 0
	v_mov_b32_e32 v30, 0
	v_mov_b32_e32 v31, 0
	v_add_u32_e32 v194, v33, v178
	v_add_u32_e32 v195, v34, v178
	v_add_u32_e32 v196, v35, v188
	s_lshl_b32 s44, s6, 1
	s_lshl_b32 s10, s7, 1
	v_add_u32_e32 v197, v37, v188
	v_lshlrev_b32_e32 v200, 2, v32
	s_waitcnt vmcnt(0)
	s_branch .LBB0_450
.LBB0_449:
	v_max_f32_e32 v49, v153, v153
	v_max_f32_e32 v49, v49, v205
	v_sub_f32_e32 v50, v201, v49
	v_mul_f32_e32 v50, 0x3fb8aa3b, v50
	v_exp_f32_e32 v72, v50
	s_waitcnt lgkmcnt(1)
	v_add_f32_e32 v50, v204, v203
	v_add_f32_e32 v71, v152, v49
	v_sub_f32_e32 v49, v201, v204
	v_mul_f32_e32 v51, 0xbfb8aa3b, v50
	v_sub_f32_e32 v50, v201, v53
	v_mul_f32_e32 v49, 0x3fb8aa3b, v49
	v_mul_f32_e32 v73, 0x3fb8aa3b, v50
	s_waitcnt lgkmcnt(0)
	v_add_f32_e32 v50, v53, v202
	v_mul_f32_e32 v53, 0xbfb8aa3b, v50
	v_exp_f32_e32 v50, v49
	v_exp_f32_e32 v76, v73
	v_exp_f32_e32 v49, v51
	v_exp_f32_e32 v51, v53
	v_fmac_f32_e32 v70, v52, v50
	ds_bpermute_b32 v52, v200, v70
	v_fmac_f32_e32 v74, v48, v76
	ds_bpermute_b32 v53, v200, v74
	s_and_b64 s[6:7], s[50:51], exec
	s_cselect_b32 s6, s92, 0x1de20
	s_waitcnt lgkmcnt(1)
	v_max_f32_e64 v48, |v52|, |v52|
	v_max_f32_e32 v48, v48, v49
	v_rcp_f32_e32 v48, v48
	s_waitcnt lgkmcnt(0)
	v_max_f32_e64 v49, |v53|, |v53|
	s_cmp_gt_u32 s11, 1
	v_max_f32_e32 v49, v49, v51
	v_pk_fma_f32 v[44:45], v[44:45], v[50:51], v[66:67] op_sel_hi:[1,0,1]
	s_cselect_b32 s8, s77, 0x23200000
	v_add_u32_e32 v74, s64, v186
	v_pk_fma_f32 v[46:47], v[46:47], v[50:51], v[68:69] op_sel_hi:[1,0,1]
	v_pk_mul_f32 v[44:45], v[44:45], v[48:49] op_sel_hi:[1,0]
	s_cselect_b32 s7, 0, 0
	s_add_u32 s8, s72, s8
	v_ashrrev_i32_e32 v75, 31, v74
	v_pk_mul_f32 v[46:47], v[46:47], v[48:49] op_sel_hi:[1,0]
	v_cvt_pk_bf16_f32 v44, v44, v45
	v_rcp_f32_e32 v52, v49
	v_cvt_pk_bf16_f32 v45, v46, v47
	s_addc_u32 s9, s73, s7
	v_lshlrev_b64 v[74:75], 10, v[74:75]
	ds_bpermute_b32 v44, v185, v44
	ds_bpermute_b32 v45, v185, v45
	v_lshl_add_u64 v[74:75], s[8:9], 0, v[74:75]
	v_lshl_add_u64 v[74:75], v[74:75], 0, s[44:45]
	s_mov_b32 s11, s45
	v_lshl_add_u64 v[74:75], v[74:75], 0, s[10:11]
	v_pk_fma_f32 v[40:41], v[40:41], v[76:77], v[62:63] op_sel_hi:[1,0,1]
	v_add_u32_e32 v78, s64, v187
	v_lshl_add_u64 v[74:75], v[74:75], 0, v[144:145]
	v_pk_fma_f32 v[42:43], v[42:43], v[76:77], v[64:65] op_sel_hi:[1,0,1]
	v_pk_mul_f32 v[40:41], v[40:41], v[52:53] op_sel_hi:[1,0]
	v_ashrrev_i32_e32 v79, 31, v78
	v_pk_mul_f32 v[42:43], v[42:43], v[52:53] op_sel_hi:[1,0]
	s_waitcnt lgkmcnt(0)
; #define LDS_BARRIER() do { asm volatile("s_waitcnt lgkmcnt(0)" ::: "memory"); __builtin_amdgcn_s_barrier(); asm volatile("" ::: "memory"); } while (0)
; __device__ __forceinline__ unsigned cvt_pk_bf16(float lo, float hi) { unsigned r; asm volatile("v_cvt_pk_bf16_f32 %0, %1, %2" : "=v"(r) : "v"(lo), "v"(hi)); return r; }
; __device__ __forceinline__ void p4_scan(const Args& a, const Frame& F) {
;     ...
;                     { bf16* HXs = store ? HX : (bf16*)(a.ws + WS_H2) - (size_t)T * 512;
;                         const int lnh = c + 16 * q, pfh = (lnh >> 2) & 15, pqh = lnh & 3, bah = 4 * (pfh + 16 * pqh);
;                         const int tokA = base + (dir ? 127 - (16 * ta + pfh) : (16 * ta + pfh)), tokB = base + (dir ? 127 - (16 * tb + pfh) : (16 * tb + pfh));
; #pragma unroll
;                         for (int mt = 0; mt < 2; ++mt) { const f32x4 vA = (acc2A[mt] + acc3A[mt] * decA) * invA, vB = (acc2B[mt] + acc3B[mt] * decB) * invB;
;                             u32x2 o; o.x = pg8::cvt_pk_bf16(vA[0], vA[1]); o.y = pg8::cvt_pk_bf16(vA[2], vA[3]);
;                             o.x = (unsigned)__builtin_amdgcn_ds_bpermute(bah, (int)o.x); o.y = (unsigned)__builtin_amdgcn_ds_bpermute(bah, (int)o.y);
;                             *(u32x2*)(HXs + (size_t)tokA * 512 + h * 128 + vs * 32 + 16 * mt + 4 * pqh) = o;
;                             o.x = pg8::cvt_pk_bf16(vB[0], vB[1]); o.y = pg8::cvt_pk_bf16(vB[2], vB[3]);
;                             o.x = (unsigned)__builtin_amdgcn_ds_bpermute(bah, (int)o.x); o.y = (unsigned)__builtin_amdgcn_ds_bpermute(bah, (int)o.y);
;                             *(u32x2*)(HXs + (size_t)tokB * 512 + h * 128 + vs * 32 + 16 * mt + 4 * pqh) = o; } }
;                 }
;                 LDS_BARRIER();
	global_store_dwordx2 v[74:75], v[44:45], off
	v_cvt_pk_bf16_f32 v40, v40, v41
	v_cvt_pk_bf16_f32 v41, v42, v43
	v_lshlrev_b64 v[78:79], 10, v[78:79]
	ds_bpermute_b32 v40, v185, v40
	ds_bpermute_b32 v41, v185, v41
	v_lshl_add_u64 v[78:79], s[8:9], 0, v[78:79]
	v_lshl_add_u64 v[78:79], v[78:79], 0, s[44:45]
	v_lshl_add_u64 v[78:79], v[78:79], 0, s[10:11]
	v_pk_fma_f32 v[36:37], v[36:37], v[50:51], v[58:59] op_sel_hi:[1,0,1]
	v_lshl_add_u64 v[78:79], v[78:79], 0, v[144:145]
	v_pk_fma_f32 v[38:39], v[38:39], v[50:51], v[60:61] op_sel_hi:[1,0,1]
	v_pk_mul_f32 v[36:37], v[36:37], v[48:49] op_sel_hi:[1,0]
	s_waitcnt lgkmcnt(0)
	global_store_dwordx2 v[78:79], v[40:41], off
	v_pk_mul_f32 v[38:39], v[38:39], v[48:49] op_sel_hi:[1,0]
	v_cvt_pk_bf16_f32 v36, v36, v37
	ds_bpermute_b32 v36, v185, v36
	v_cvt_pk_bf16_f32 v37, v38, v39
	ds_bpermute_b32 v37, v185, v37
	v_pk_fma_f32 v[32:33], v[32:33], v[76:77], v[54:55] op_sel_hi:[1,0,1]
	v_pk_fma_f32 v[34:35], v[34:35], v[76:77], v[56:57] op_sel_hi:[1,0,1]
	v_pk_mul_f32 v[32:33], v[32:33], v[52:53] op_sel_hi:[1,0]
	v_pk_mul_f32 v[34:35], v[34:35], v[52:53] op_sel_hi:[1,0]
	s_waitcnt lgkmcnt(0)
	global_store_dwordx2 v[74:75], v[36:37], off offset:32
	v_cvt_pk_bf16_f32 v32, v32, v33
	v_cvt_pk_bf16_f32 v33, v34, v35
	ds_bpermute_b32 v32, v185, v32
	ds_bpermute_b32 v33, v185, v33
	v_add_u32_e32 v36, s6, v189
	s_add_i32 s6, s35, 0
	v_add_u32_e32 v73, s6, v172
	v_pk_mul_f32 v[10:11], v[10:11], v[72:73] op_sel_hi:[1,0]
	s_waitcnt lgkmcnt(0)
	global_store_dwordx2 v[78:79], v[32:33], off offset:32
	s_waitcnt lgkmcnt(0)
	s_barrier
; #define LAS __attribute__((address_space(3)))
; __device__ __forceinline__ unsigned pk2(float lo, float hi) { return f2bf(lo) | (f2bf(hi) << 16); }
; #define LDS_BARRIER() do { asm volatile("s_waitcnt lgkmcnt(0)" ::: "memory"); __builtin_amdgcn_s_barrier(); asm volatile("" ::: "memory"); } while (0)
; __device__ __forceinline__ void p4_scan(const Args& a, const Frame& F) {
;     ...
;                 {
;                     bf16x8 vf[3][4];
; #pragma unroll
;                     for (int nt = 0; nt < 3; ++nt)
; #pragma unroll
;                         for (int ks = 0; ks < 4; ++ks) vf[nt][ks] = *(const LAS bf16x8*)(L + vacur + (16 * nt + c) * SP + (ks * 32 + q * 8) * 2);
; #pragma unroll
;                     for (int d2 = 0; d2 < 2; ++d2) {
;                         unsigned ka[8];
; #pragma unroll
;                         for (int i = 0; i < 8; ++i) ka[i] = Lb + (unsigned)kcur + kadA[i] + (d2 ? 32u : 0u);
;                         u32x2 kr[8]; tr_read_k8(kr, ka);
; #pragma unroll
;                         for (int nt = 0; nt < 3; ++nt) accC[d2][nt] = accC[d2][nt] * cd;
; #pragma unroll
;                         for (int ks = 0; ks < 4; ++ks) { const bf16x8 af = mk_frag(kr[ks * 2], kr[ks * 2 + 1]);
; #pragma unroll
;                             for (int nt = 0; nt < 3; ++nt) accC[d2][nt] = __builtin_amdgcn_mfma_f32_16x16x32_bf16(af, vf[nt][ks], accC[d2][nt], 0, 0, 0); }
; #pragma unroll
;                         for (int nt = 0; nt < 3; ++nt) { u32x2 o; o.x = pk2(accC[d2][nt][0], accC[d2][nt][1]); o.y = pk2(accC[d2][nt][2], accC[d2][nt][3]);
;                             *(LAS u32x2*)(L + S_CT + (16 * nt + c) * SP + (16 * (2 * w + d2) + 4 * q) * 2) = o; }
;                     }
;                 }
;                 mcar = mnew;
;                 btot = pbt; pmx = ppx;
;                 LDS_BARRIER();
	v_pk_mul_f32 v[8:9], v[8:9], v[72:73] op_sel_hi:[1,0]
	ds_read_b128 v[52:55], v36
	ds_read_b128 v[56:59], v36 offset:64
	ds_read_b128 v[44:47], v36 offset:128
	ds_read_b128 v[32:35], v36 offset:192
	ds_read_b128 v[60:63], v36 offset:4352
	ds_read_b128 v[64:67], v36 offset:4416
	ds_read_b128 v[48:51], v36 offset:4480
	ds_read_b128 v[40:43], v36 offset:4544
	ds_read_b128 v[74:77], v36 offset:8704
	ds_read_b128 v[78:81], v36 offset:8768
	ds_read_b128 v[82:85], v36 offset:8832
	ds_read_b128 v[36:39], v36 offset:8896
	v_add_u32_e32 v68, s6, v148
	v_add_u32_e32 v69, s6, v149
	v_add_u32_e32 v70, s6, v171
	v_add_u32_e32 v102, s6, v173
	v_add_u32_e32 v103, s6, v174
	v_add_u32_e32 v104, s6, v175
	v_add_u32_e32 v105, s6, v176
	ds_read_b64_tr_b16 v[98:99], v68
	ds_read_b64_tr_b16 v[100:101], v69
	ds_read_b64_tr_b16 v[94:95], v70
	ds_read_b64_tr_b16 v[96:97], v73
	ds_read_b64_tr_b16 v[90:91], v102
	ds_read_b64_tr_b16 v[92:93], v103
	ds_read_b64_tr_b16 v[86:87], v104
	ds_read_b64_tr_b16 v[88:89], v105
	s_waitcnt lgkmcnt(0)
	v_pk_mul_f32 v[14:15], v[14:15], v[72:73] op_sel_hi:[1,0]
	s_waitcnt lgkmcnt(11)
	v_mfma_f32_16x16x32_bf16 v[8:11], v[98:101], v[52:55], v[8:11]
	v_mul_f32_e64 v12, v12, v72
	v_mul_f32_e64 v13, v13, v72
	v_pk_mul_f32 v[18:19], v[18:19], v[72:73] op_sel_hi:[1,0]
	v_pk_mul_f32 v[16:17], v[16:17], v[72:73] op_sel_hi:[1,0]
	s_waitcnt lgkmcnt(10)
	v_mfma_f32_16x16x32_bf16 v[8:11], v[94:97], v[56:59], v[8:11]
	s_add_i32 s6, s6, 32
	v_add_u32_e32 v73, s6, v172
	v_pk_mul_f32 v[22:23], v[22:23], v[72:73] op_sel_hi:[1,0]
	s_waitcnt lgkmcnt(7)
	v_mfma_f32_16x16x32_bf16 v[12:15], v[98:101], v[60:63], v[12:15]
	v_mul_f32_e64 v20, v20, v72
	v_mul_f32_e64 v21, v21, v72
	v_add_u32_e32 v102, s6, v173
	v_add_u32_e32 v103, s6, v174
	v_mfma_f32_16x16x32_bf16 v[8:11], v[90:93], v[44:47], v[8:11]
	v_add_u32_e32 v104, s6, v175
	v_add_u32_e32 v105, s6, v176
	v_pk_mul_f32 v[26:27], v[26:27], v[72:73] op_sel_hi:[1,0]
	s_waitcnt lgkmcnt(6)
	v_mfma_f32_16x16x32_bf16 v[12:15], v[94:97], v[64:67], v[12:15]
	v_mul_f32_e64 v24, v24, v72
	v_mul_f32_e64 v25, v25, v72
	v_pk_mul_f32 v[30:31], v[30:31], v[72:73] op_sel_hi:[1,0]
	v_pk_mul_f32 v[28:29], v[28:29], v[72:73] op_sel_hi:[1,0]
	v_mfma_f32_16x16x32_bf16 v[8:11], v[86:89], v[32:35], v[8:11]
	s_cmpk_eq_i32 s34, 0x42
	v_mov_b32_e32 v201, v71
	s_mov_b32 s11, s34
	s_waitcnt lgkmcnt(3)
	v_mfma_f32_16x16x32_bf16 v[16:19], v[98:101], v[74:77], v[16:19]
	s_waitcnt vmcnt(4)
	v_mov_b64_e32 v[152:153], v[150:151]
	s_nop 0
	v_bfe_u32 v68, v8, 16, 1
	v_add3_u32 v68, v8, v68, s93
	v_mfma_f32_16x16x32_bf16 v[12:15], v[90:93], v[48:51], v[12:15]
	v_bfe_u32 v69, v9, 16, 1
	v_lshrrev_b32_e32 v68, 16, v68
	v_add3_u32 v69, v9, v69, s93
	s_waitcnt lgkmcnt(2)
	v_mfma_f32_16x16x32_bf16 v[16:19], v[94:97], v[78:81], v[16:19]
	v_and_or_b32 v68, v69, s94, v68
	v_bfe_u32 v69, v10, 16, 1
	v_add3_u32 v69, v10, v69, s93
	v_mfma_f32_16x16x32_bf16 v[12:15], v[86:89], v[40:43], v[12:15]
	v_bfe_u32 v70, v11, 16, 1
	v_lshrrev_b32_e32 v69, 16, v69
	v_add3_u32 v70, v11, v70, s93
	s_waitcnt lgkmcnt(1)
	v_mfma_f32_16x16x32_bf16 v[16:19], v[90:93], v[82:85], v[16:19]
	v_and_or_b32 v69, v70, s94, v69
	ds_write_b64 v197, v[68:69]
	s_nop 0
	v_bfe_u32 v68, v12, 16, 1
	v_add3_u32 v68, v12, v68, s93
	v_bfe_u32 v69, v13, 16, 1
	v_lshrrev_b32_e32 v68, 16, v68
	v_add3_u32 v69, v13, v69, s93
	s_waitcnt lgkmcnt(1)
	v_mfma_f32_16x16x32_bf16 v[16:19], v[86:89], v[36:39], v[16:19]
	v_and_or_b32 v68, v69, s94, v68
	v_bfe_u32 v69, v14, 16, 1
	v_add3_u32 v69, v14, v69, s93
	v_bfe_u32 v70, v15, 16, 1
	v_lshrrev_b32_e32 v69, 16, v69
	v_add3_u32 v70, v15, v70, s93
	v_and_or_b32 v69, v70, s94, v69
	ds_write_b64 v197, v[68:69] offset:4352
	v_bfe_u32 v68, v16, 16, 1
	v_add3_u32 v68, v16, v68, s93
	v_bfe_u32 v69, v17, 16, 1
	v_lshrrev_b32_e32 v68, 16, v68
	v_add3_u32 v69, v17, v69, s93
	v_and_or_b32 v68, v69, s94, v68
	v_bfe_u32 v69, v18, 16, 1
	v_add3_u32 v69, v18, v69, s93
	v_bfe_u32 v70, v19, 16, 1
	v_lshrrev_b32_e32 v69, 16, v69
	v_add3_u32 v70, v19, v70, s93
	v_and_or_b32 v69, v70, s94, v69
	ds_write_b64 v197, v[68:69] offset:8704
	v_add_u32_e32 v68, s6, v148
	v_add_u32_e32 v69, s6, v149
	v_add_u32_e32 v70, s6, v171
	ds_read_b64_tr_b16 v[98:99], v68
	ds_read_b64_tr_b16 v[100:101], v69
	ds_read_b64_tr_b16 v[94:95], v70
	ds_read_b64_tr_b16 v[96:97], v73
	ds_read_b64_tr_b16 v[90:91], v102
	ds_read_b64_tr_b16 v[92:93], v103
	ds_read_b64_tr_b16 v[86:87], v104
	ds_read_b64_tr_b16 v[88:89], v105
	s_waitcnt lgkmcnt(0)
	s_nop 0
	v_mfma_f32_16x16x32_bf16 v[20:23], v[98:101], v[52:55], v[20:23]
	v_mfma_f32_16x16x32_bf16 v[20:23], v[94:97], v[56:59], v[20:23]
	v_mfma_f32_16x16x32_bf16 v[24:27], v[98:101], v[60:63], v[24:27]
	v_mfma_f32_16x16x32_bf16 v[20:23], v[90:93], v[44:47], v[20:23]
	v_mfma_f32_16x16x32_bf16 v[24:27], v[94:97], v[64:67], v[24:27]
	v_mfma_f32_16x16x32_bf16 v[20:23], v[86:89], v[32:35], v[20:23]
	v_mfma_f32_16x16x32_bf16 v[28:31], v[98:101], v[74:77], v[28:31]
	v_mfma_f32_16x16x32_bf16 v[24:27], v[90:93], v[48:51], v[24:27]
	s_nop 5
	v_bfe_u32 v32, v20, 16, 1
	v_add3_u32 v32, v20, v32, s93
	v_bfe_u32 v33, v21, 16, 1
	v_mfma_f32_16x16x32_bf16 v[28:31], v[94:97], v[78:81], v[28:31]
	v_lshrrev_b32_e32 v32, 16, v32
	v_add3_u32 v33, v21, v33, s93
	v_and_or_b32 v32, v33, s94, v32
	v_mfma_f32_16x16x32_bf16 v[24:27], v[86:89], v[40:43], v[24:27]
	v_bfe_u32 v33, v22, 16, 1
	v_add3_u32 v33, v22, v33, s93
	v_bfe_u32 v34, v23, 16, 1
	v_lshrrev_b32_e32 v33, 16, v33
	v_add3_u32 v34, v23, v34, s93
	v_mfma_f32_16x16x32_bf16 v[28:31], v[90:93], v[82:85], v[28:31]
	v_and_or_b32 v33, v34, s94, v33
	ds_write_b64 v197, v[32:33] offset:32
	v_bfe_u32 v32, v24, 16, 1
	v_add3_u32 v32, v24, v32, s93
	v_bfe_u32 v33, v25, 16, 1
	v_lshrrev_b32_e32 v32, 16, v32
	v_add3_u32 v33, v25, v33, s93
	v_mfma_f32_16x16x32_bf16 v[28:31], v[86:89], v[36:39], v[28:31]
	v_and_or_b32 v32, v33, s94, v32
	v_bfe_u32 v33, v26, 16, 1
	v_add3_u32 v33, v26, v33, s93
	v_bfe_u32 v34, v27, 16, 1
	v_lshrrev_b32_e32 v33, 16, v33
	v_add3_u32 v34, v27, v34, s93
	v_and_or_b32 v33, v34, s94, v33
	ds_write_b64 v197, v[32:33] offset:4384
	v_bfe_u32 v32, v28, 16, 1
	v_add3_u32 v32, v28, v32, s93
	v_bfe_u32 v33, v29, 16, 1
	v_lshrrev_b32_e32 v32, 16, v32
	v_add3_u32 v33, v29, v33, s93
	v_and_or_b32 v32, v33, s94, v32
	v_bfe_u32 v33, v30, 16, 1
	v_add3_u32 v33, v30, v33, s93
	v_bfe_u32 v34, v31, 16, 1
	v_lshrrev_b32_e32 v33, 16, v33
	v_add3_u32 v34, v31, v34, s93
	v_and_or_b32 v33, v34, s94, v33
	ds_write_b64 v197, v[32:33] offset:8736
	s_waitcnt lgkmcnt(0)
	s_barrier
	s_cbranch_scc1 .LBB0_472

; #define LAS __attribute__((address_space(3)))
; #define LDS_WAIT() asm volatile("s_waitcnt lgkmcnt(0)" ::: "memory")
; __device__ __forceinline__ void p4_scan(const Args& a, const Frame& F) {
;     ...
;                 const int base = chunk_base(ci); const bool store = ci >= 2, more = ci + 1 < 66;
;                 const int kcur = (ci & 1) ? S_K1 : S_K0, vacur = (ci & 1) ? S_VA1 : S_VA0;
;                 const float M127 = fmaxf(pmx, mcar), cd = __expf(mcar - M127), mnew = btot + M127;
;                 { const int basen = chunk_base(more ? ci + 1 : ci); pbt = CH[(hd * 528 + (basen >> 7)) * 2]; ppx = CH[(hd * 528 + (basen >> 7)) * 2 + 1]; }
;                 bf16x8 qfA[4], qfB[4];
;                 f32x4 acc3A[3], acc3B[3];
;                 {
;                     bf16x8 cf[3][4];
; #pragma unroll
;                     for (int ks = 0; ks < 4; ++ks) { qfA[ks] = *(const LAS bf16x8*)(L + S_QS + trA * SP + (ks * 32 + q * 8) * 2); qfB[ks] = *(const LAS bf16x8*)(L + S_QS + trB * SP + (ks * 32 + q * 8) * 2); }
; #pragma unroll
;                     for (int mt = 0; mt < 3; ++mt)
; #pragma unroll
;                         for (int ks = 0; ks < 4; ++ks) cf[mt][ks] = *(const LAS bf16x8*)(L + S_CT + (16 * mt + c) * SP + (ks * 32 + q * 8) * 2);
;                     LDS_WAIT(); __builtin_amdgcn_sched_barrier(0);
; #pragma unroll
;                     for (int mt = 0; mt < 3; ++mt) { acc3A[mt] = (f32x4){0.f, 0.f, 0.f, 0.f}; acc3B[mt] = (f32x4){0.f, 0.f, 0.f, 0.f};
; #pragma unroll
;                         for (int ks = 0; ks < 4; ++ks) { acc3A[mt] = __builtin_amdgcn_mfma_f32_16x16x32_bf16(cf[mt][ks], qfA[ks], acc3A[mt], 0, 0, 0); acc3B[mt] = __builtin_amdgcn_mfma_f32_16x16x32_bf16(cf[mt][ks], qfB[ks], acc3B[mt], 0, 0, 0); } }
;                 }
;                 const float MtA = fmaxf(PML[trA], mcar), MtB = fmaxf(PML[trB], mcar);
;                 const float decA = __expf(mcar - MtA), emtA = __expf(-(BL[trA] + MtA)), decB = __expf(mcar - MtB), emtB = __expf(-(BL[trB] + MtB));
;                 {
;                     bf16x8 kf[2][4];
; #pragma unroll
;                     for (int u = 0; u < 2; ++u)
; #pragma unroll
;                         for (int ks = 0; ks < 4; ++ks) kf[u][ks] = *(const LAS bf16x8*)(L + kcur + (16 * u + c) * SP + (ks * 32 + q * 8) * 2);
.LBB0_454:
	s_add_i32 s34, s11, 1
	s_bitcmp0_b32 s11, 0
	s_cselect_b64 s[50:51], -1, 0
	s_and_b64 s[6:7], s[50:51], exec
	s_cselect_b32 s35, s91, 0x11000
	s_cmpk_eq_i32 s11, 0x41
	s_cselect_b32 s8, s11, s34
	s_sub_i32 s52, 0x41, s8
	v_sub_co_u32_e64 v32, s[6:7], s8, 2
	s_and_b64 s[8:9], s[4:5], exec
	v_readfirstlane_b32 s8, v32
	s_cselect_b32 s8, s8, s52
	s_lshl_b32 s8, s8, 7
	s_add_i32 s8, s8, s33
	s_and_b64 s[6:7], s[6:7], exec
	s_cselect_b32 s6, s88, s8
	s_ashr_i32 s6, s6, 7
	s_add_i32 s6, s6, s76
	s_lshl_b32 s6, s6, 1
	s_ashr_i32 s7, s6, 31
	s_lshl_b64 s[6:7], s[6:7], 2
	s_add_u32 s6, s60, s6
	s_addc_u32 s7, s61, s7
	global_load_dwordx2 v[150:151], v145, s[6:7]
	ds_read_b128 v[56:59], v194
	ds_read_b128 v[60:63], v194 offset:64
	ds_read_b128 v[64:67], v195
	ds_read_b128 v[68:71], v195 offset:64
	ds_read_b128 v[72:75], v194 offset:128
	ds_read_b128 v[76:79], v194 offset:192
	ds_read_b128 v[80:83], v195 offset:128
	ds_read_b128 v[84:87], v195 offset:192
	ds_read_b128 v[32:35], v196
	ds_read_b128 v[36:39], v196 offset:64
	ds_read_b128 v[40:43], v196 offset:128
	ds_read_b128 v[48:51], v196 offset:192
	ds_read_b128 v[52:55], v196 offset:4352
	ds_read_b128 v[88:91], v196 offset:4416
	ds_read_b128 v[92:95], v196 offset:4480
	ds_read_b128 v[96:99], v196 offset:4544
	ds_read_b128 v[100:103], v196 offset:8704
	ds_read_b128 v[104:107], v196 offset:8768
	ds_read_b128 v[108:111], v196 offset:8832
	ds_read_b128 v[112:115], v196 offset:8896
	s_waitcnt lgkmcnt(11)
	v_mfma_f32_16x16x32_bf16 v[44:47], v[32:35], v[56:59], 0
	v_max_f32_e32 v205, v201, v201
	s_andn2_b64 vcc, exec, s[42:43]
	v_mfma_f32_16x16x32_bf16 v[32:35], v[32:35], v[64:67], 0
	s_waitcnt lgkmcnt(10)
	v_mfma_f32_16x16x32_bf16 v[44:47], v[36:39], v[60:63], v[44:47]
	v_mfma_f32_16x16x32_bf16 v[32:35], v[36:39], v[68:71], v[32:35]
	s_waitcnt lgkmcnt(9)
	v_mfma_f32_16x16x32_bf16 v[36:39], v[40:43], v[72:75], v[44:47]
	v_mfma_f32_16x16x32_bf16 v[32:35], v[40:43], v[80:83], v[32:35]
	s_waitcnt lgkmcnt(8)
	v_mfma_f32_16x16x32_bf16 v[44:47], v[48:51], v[76:79], v[36:39]
	v_mfma_f32_16x16x32_bf16 v[40:43], v[48:51], v[84:87], v[32:35]
	s_waitcnt lgkmcnt(7)
	v_mfma_f32_16x16x32_bf16 v[32:35], v[52:55], v[56:59], 0
	v_mfma_f32_16x16x32_bf16 v[36:39], v[52:55], v[64:67], 0
	s_waitcnt lgkmcnt(6)
	v_mfma_f32_16x16x32_bf16 v[32:35], v[88:91], v[60:63], v[32:35]
	v_mfma_f32_16x16x32_bf16 v[36:39], v[88:91], v[68:71], v[36:39]
	s_waitcnt lgkmcnt(5)
	v_mfma_f32_16x16x32_bf16 v[32:35], v[92:95], v[72:75], v[32:35]
	v_mfma_f32_16x16x32_bf16 v[48:51], v[92:95], v[80:83], v[36:39]
	ds_read_b32 v92, v179
	ds_read_b32 v93, v180
	ds_read_b32 v203, v181
	ds_read_b32 v202, v182
	s_waitcnt lgkmcnt(8)
	v_mfma_f32_16x16x32_bf16 v[36:39], v[96:99], v[76:79], v[32:35]
	v_mfma_f32_16x16x32_bf16 v[32:35], v[96:99], v[84:87], v[48:51]
	s_waitcnt lgkmcnt(7)
	v_mfma_f32_16x16x32_bf16 v[48:51], v[100:103], v[56:59], 0
	v_mfma_f32_16x16x32_bf16 v[52:55], v[100:103], v[64:67], 0
	s_waitcnt lgkmcnt(6)
	v_mfma_f32_16x16x32_bf16 v[48:51], v[104:107], v[60:63], v[48:51]
	v_mfma_f32_16x16x32_bf16 v[52:55], v[104:107], v[68:71], v[52:55]
	s_waitcnt lgkmcnt(5)
	v_mfma_f32_16x16x32_bf16 v[48:51], v[108:111], v[72:75], v[48:51]
	v_mfma_f32_16x16x32_bf16 v[88:91], v[108:111], v[80:83], v[52:55]
	s_waitcnt lgkmcnt(3)
	s_nop 3
	v_max_f32_e32 v52, v92, v92
	v_max_f32_e32 v204, v52, v205
	v_mfma_f32_16x16x32_bf16 v[52:55], v[112:115], v[76:79], v[48:51]
	s_waitcnt lgkmcnt(2)
	v_max_f32_e32 v92, v93, v93
	s_nop 0
	v_cndmask_b32_e64 v48, 0, 1, s[42:43]
	v_cmp_ne_u32_e64 s[6:7], 1, v48
	v_mfma_f32_16x16x32_bf16 v[48:51], v[112:115], v[84:87], v[88:91]
	s_nop 1
	v_max_f32_e32 v53, v92, v205
	s_cbranch_vccnz .LBB0_467
	s_nop 3
	v_add3_u32 v49, v183, s35, v188
	ds_read_b128 v[116:119], v49 offset:4544
	ds_read_b128 v[112:115], v49 offset:4480
	ds_read_b128 v[108:111], v49 offset:4416
	ds_read_b128 v[104:107], v49 offset:4352
	ds_read_b128 v[100:103], v49 offset:192
	ds_read_b128 v[88:91], v49 offset:128
	ds_read_b128 v[92:95], v49 offset:64
	ds_read_b128 v[96:99], v49
	v_add_u32_e32 v49, s35, v192
	s_mov_b32 s86, 0
	v_mov_b32_e32 v50, v178
	v_mov_b32_e32 v51, v191
	v_mov_b32_e32 v54, v190
	v_mov_b32_e32 v55, v184
	s_branch .LBB0_457

; #define LAS __attribute__((address_space(3)))
; __device__ __forceinline__ void p4_scan(const Args& a, const Frame& F) {
;     ...
;                         if (pr + 1 < npB) {
; #pragma unroll
;                             for (int u = 0; u < 2; ++u)
; #pragma unroll
;                                 for (int ks = 0; ks < 4; ++ks) kf[u][ks] = *(const LAS bf16x8*)(L + kcur + (16 * (2 * pr + 2 + u) + c) * SP + (ks * 32 + q * 8) * 2);
;                         }
.LBB0_461:
	s_add_i32 s86, s86, 1
	s_cmp_lt_u32 s86, s79
	s_cbranch_scc0 .LBB0_463
	v_add_u32_e32 v116, 0, v49
	ds_read_b128 v[96:99], v116
	ds_read_b128 v[92:95], v116 offset:64
	ds_read_b128 v[88:91], v116 offset:128
	ds_read_b128 v[100:103], v116 offset:192
	ds_read_b128 v[104:107], v116 offset:4352
	ds_read_b128 v[108:111], v116 offset:4416
	ds_read_b128 v[112:115], v116 offset:4480
	ds_read_b128 v[116:119], v116 offset:4544
	s_waitcnt lgkmcnt(8)
	s_branch .Ls463b

; #define LAS __attribute__((address_space(3)))
; __device__ __forceinline__ unsigned cvt_pk_bf16(float lo, float hi) { unsigned r; asm volatile("v_cvt_pk_bf16_f32 %0, %1, %2" : "=v"(r) : "v"(lo), "v"(hi)); return r; }
; __device__ __forceinline__ void p4_scan(const Args& a, const Frame& F) {
;     ...
;                         for (int u = 0; u < 2; ++u) { const int s0 = 16 * (2 * pr + u) + 4 * q;
;                             float r[4];
; #pragma unroll
;                             for (int j = 0; j < 4; ++j) r[j] = (s0 + j <= trB) ? apB[u][j] * __expf(glv[u][j] - MtB) : 0.f;
;                             u32x2 o; o.x = pg8::cvt_pk_bf16(r[0], r[1]); o.y = pg8::cvt_pk_bf16(r[2], r[3]);
;                             *(LAS u32x2*)(L + S_QS + trB * SP + s0 * 2) = o;
;                             if (doA) {
; #pragma unroll
;                                 for (int j = 0; j < 4; ++j) r[j] = (s0 + j <= trA) ? apA[u][j] * __expf(glv[u][j] - MtA) : 0.f;
;                                 o.x = pg8::cvt_pk_bf16(r[0], r[1]); o.y = pg8::cvt_pk_bf16(r[2], r[3]);
;                                 *(LAS u32x2*)(L + S_QS + trA * SP + s0 * 2) = o; } }
.Ls463b:
	v_sub_f32_e32 v198, v128, v53
	v_mul_f32_e32 v198, 0x3fb8aa3b, v198
	v_exp_f32_e32 v198, v198
	v_sub_f32_e32 v199, v129, v53
	v_mul_f32_e32 v199, 0x3fb8aa3b, v199
	v_exp_f32_e32 v199, v199
	v_mul_f32_e32 v140, v198, v140
	v_sub_f32_e32 v198, v130, v53
	v_mul_f32_e32 v198, 0x3fb8aa3b, v198
	v_exp_f32_e32 v198, v198
	v_cmp_le_i32_e32 vcc, v55, v177
	v_mul_f32_e32 v141, v199, v141
	v_add_u32_e32 v206, 2, v55
	v_mul_f32_e32 v142, v198, v142
	v_sub_f32_e32 v198, v131, v53
	v_mul_f32_e32 v198, 0x3fb8aa3b, v198
	v_exp_f32_e32 v198, v198
	v_cndmask_b32_e32 v140, 0, v140, vcc
	v_cmp_lt_i32_e32 vcc, v55, v177
	v_mul_f32_e32 v143, v198, v143
	s_nop 0
	v_cndmask_b32_e32 v141, 0, v141, vcc
	v_cmp_le_i32_e32 vcc, v206, v177
	v_cvt_pk_bf16_f32 v210, v140, v141
	v_add_u32_e32 v141, 0, v51
	v_add_u32_e32 v140, 0, v54
	v_cndmask_b32_e32 v199, 0, v142, vcc
	v_add_u32_e32 v142, 3, v55
	v_cmp_le_i32_e32 vcc, v142, v177
	s_nop 1
	v_cndmask_b32_e32 v143, 0, v143, vcc
	s_and_b64 vcc, exec, s[8:9]
	v_cvt_pk_bf16_f32 v211, v199, v143
	ds_write_b64 v141, v[210:211]
	s_cbranch_vccnz .LBB0_465
	v_sub_f32_e32 v128, v128, v204
	v_mul_f32_e32 v128, 0x3fb8aa3b, v128
	v_sub_f32_e32 v129, v129, v204
	v_exp_f32_e32 v128, v128
	v_mul_f32_e32 v129, 0x3fb8aa3b, v129
	v_sub_f32_e32 v130, v130, v204
	v_exp_f32_e32 v129, v129
	v_mul_f32_e32 v130, 0x3fb8aa3b, v130
	v_sub_f32_e32 v131, v131, v204
	v_exp_f32_e32 v130, v130
	v_mul_f32_e32 v131, 0x3fb8aa3b, v131
	v_exp_f32_e32 v131, v131
	v_mul_f32_e32 v128, v128, v136
	v_cmp_le_i32_e32 vcc, v55, v147
	v_mul_f32_e32 v129, v129, v137
	v_mul_f32_e32 v130, v130, v138
	v_cndmask_b32_e32 v128, 0, v128, vcc
	v_cmp_lt_i32_e32 vcc, v55, v147
	v_mul_f32_e32 v131, v131, v139
	s_nop 0
	v_cndmask_b32_e32 v129, 0, v129, vcc
	v_cmp_le_i32_e32 vcc, v206, v147
	v_cvt_pk_bf16_f32 v128, v128, v129
	s_nop 1
	v_cndmask_b32_e32 v130, 0, v130, vcc
	v_cmp_le_i32_e32 vcc, v142, v147
	s_nop 1
	v_cndmask_b32_e32 v131, 0, v131, vcc
	v_cvt_pk_bf16_f32 v129, v130, v131
	ds_write_b64 v140, v[128:129]
